# union8 + widen GEMM K-loop: same scalar relax-flag simplification (all five GEMM K-loops now)
# speedup vs baseline: 1.0080x; 1.0028x over previous
; #define PG8_STAGE(bufoff, gbase, voff) do { _Pragma("unroll") for (int _i = 0; _i < 2; ++_i) \
;         __builtin_amdgcn_global_load_lds((const unsigned*)((const char*)(gbase) + (voff)[_i]), (PG8_LAS unsigned*)(lds + (bufoff) + ldsw + _i * 8192), 16, 0, 0); } while (0)
; #define PG8_LDA(dst, b, h) do { _Pragma("unroll") for (int m = 0; m < 4; ++m) _Pragma("unroll") for (int k = 0; k < 2; ++k) dst[m][k] = *(const PG8_LAS bf16x8*)(lds + PG8_SA(b, h) + aoff + m * 2048 + k * 1024); } while (0)
; #define PG8_LDB(dst, b, h) do { _Pragma("unroll") for (int n = 0; n < 2; ++n) _Pragma("unroll") for (int k = 0; k < 2; ++k) dst[n][k] = *(const PG8_LAS bf16x8*)(lds + PG8_SB(b, h) + boff + n * 2048 + k * 1024); } while (0)
; #define PG8_MMA(ai, bj, At, Bt) do { __builtin_amdgcn_s_setprio(1); _Pragma("unroll") for (int m = 0; m < 4; ++m) _Pragma("unroll") for (int n = 0; n < 2; ++n) _Pragma("unroll") for (int k = 0; k < 2; ++k) \
;         acc[ai][bj][m][n] = mma16(Bt[n][k], At[m][k], acc[ai][bj][m][n]); __builtin_amdgcn_s_setprio(0); } while (0)
; #define PG8_WAIT_V(n) asm volatile("s_waitcnt vmcnt(" #n ")" ::: "memory")
; #define PG8_WAIT_VN(n) asm volatile("s_waitcnt vmcnt(%0)" :: "n"(n) : "memory")
; #define PG8_WAIT_L(n) asm volatile("s_waitcnt lgkmcnt(" #n ")" ::: "memory")
; #define PG8_BAR __builtin_amdgcn_s_barrier()
; #define PG8_SCHED __builtin_amdgcn_sched_barrier(0)
; template <class Epi, class Sched, bool ALIGN_EPI = false, bool SP2 = false>
; __device__ __forceinline__ void gemm_phase(PG8_LAS unsigned char* lds, const Gemm g, const Sched& S, const Epi& E, Stopwatch& sw) {
;     ...
;             int relax = __builtin_amdgcn_readfirstlane((int)((ui > 0) && (t == 0))); asm volatile("" : "+s"(relax));
;             PG8_LDB(B0, 0, 0); PG8_LDB(B1, 0, 1); PG8_SCHED; PG8_LDA(At, 0, 0); if (!relax) PG8_STAGE(PG8_SA(1, 1), a1 + hstep, voffA);
;             if (relax) PG8_WAIT_VN(8 + Epi::NST); else PG8_WAIT_V(8); PG8_WAIT_L(0); PG8_BAR; PG8_MMA(0, 0, At, B0); PG8_MMA(0, 1, At, B1); PG8_BAR; PG8_SCHED;
.LBB0_777:
	s_cmp_eq_u32 s58, 0
	s_cselect_b64 s[42:43], -1, 0
	s_and_b64 s[68:69], s[56:57], s[42:43]
	v_add_u32_e32 v2, 0x10000, v248
	ds_read_b128 v[150:153], v2
	ds_read_b128 v[154:157], v2 offset:1024
	ds_read_b128 v[158:161], v2 offset:2048
	ds_read_b128 v[162:165], v2 offset:3072
	v_add_u32_e32 v2, 0x14000, v248
	ds_read_b128 v[134:137], v2
	ds_read_b128 v[138:141], v2 offset:1024
	ds_read_b128 v[142:145], v2 offset:2048
	ds_read_b128 v[146:149], v2 offset:3072
	ds_read_b128 v[190:193], v249
	ds_read_b128 v[194:197], v249 offset:1024
	ds_read_b128 v[182:185], v249 offset:2048
	ds_read_b128 v[186:189], v249 offset:3072
	ds_read_b128 v[174:177], v249 offset:4096
	ds_read_b128 v[178:181], v249 offset:5120
	ds_read_b128 v[166:169], v249 offset:6144
	ds_read_b128 v[170:173], v249 offset:7168
	s_and_b64 vcc, exec, s[68:69]
	s_cbranch_vccz .LBB0_791
	s_waitcnt vmcnt(24)
	s_cbranch_execnz .LBB0_780
